# D2 plus gate/up gather offsets hoisted, unconditional loads with invalid rows clamped to the tile's first slot (no unwritten memory touched)
# speedup vs baseline: 1.0052x; 1.0052x over previous
.LBB0_780:
	v_cndmask_b32_e64 v0, 0, 1, s[38:39]
	v_cmp_ne_u32_e64 s[2:3], 1, v0
	s_andn2_b64 vcc, exec, s[38:39]
	v_mov_b32_e32 v158, v140
	v_mov_b32_e32 v155, v134
	v_mov_b32_e32 v156, v136
	v_mov_b32_e32 v157, v138
	s_cbranch_vccnz .LBB0_790
	v_add_u32_e32 v200, s62, v146
	v_cmp_gt_i32_e32 vcc, s63, v146
	v_mov_b32_e32 v201, s62
	s_nop 0
	v_cndmask_b32_e32 v200, v201, v200, vcc
	v_ashrrev_i32_e32 v201, 31, v200
	v_lshl_add_u64 v[200:201], v[200:201], 2, s[8:9]
	v_add_u32_e32 v202, s62, v147
	v_cmp_gt_i32_e32 vcc, s63, v147
	v_mov_b32_e32 v203, s62
	s_nop 0
	v_cndmask_b32_e32 v202, v203, v202, vcc
	v_ashrrev_i32_e32 v203, 31, v202
	v_lshl_add_u64 v[202:203], v[202:203], 2, s[8:9]
	v_add_u32_e32 v204, s62, v148
	v_cmp_gt_i32_e32 vcc, s63, v148
	v_mov_b32_e32 v205, s62
	s_nop 0
	v_cndmask_b32_e32 v204, v205, v204, vcc
	v_ashrrev_i32_e32 v205, 31, v204
	v_lshl_add_u64 v[204:205], v[204:205], 2, s[8:9]
	v_add_u32_e32 v206, s62, v149
	v_cmp_gt_i32_e32 vcc, s63, v149
	v_mov_b32_e32 v207, s62
	s_nop 0
	v_cndmask_b32_e32 v206, v207, v206, vcc
	v_ashrrev_i32_e32 v207, 31, v206
	v_lshl_add_u64 v[206:207], v[206:207], 2, s[8:9]
	global_load_dword v208, v[200:201], off
	global_load_dword v209, v[202:203], off
	global_load_dword v210, v[204:205], off
	global_load_dword v211, v[206:207], off
	s_waitcnt vmcnt(0)
	v_lshlrev_b32_e32 v208, 10, v208
	v_lshlrev_b32_e32 v209, 10, v209
	v_lshlrev_b32_e32 v210, 10, v210
	v_lshlrev_b32_e32 v211, 10, v211
	v_and_b32_e32 v208, 0x3fff800, v208
	v_and_b32_e32 v209, 0x3fff800, v209
	v_and_b32_e32 v210, 0x3fff800, v210
	v_and_b32_e32 v211, 0x3fff800, v211
	v_cmp_gt_i32_e32 vcc, s63, v146
	s_nop 1
	v_cndmask_b32_e32 v0, 0, v208, vcc
	v_cmp_gt_i32_e32 vcc, s63, v147
	s_nop 1
	v_cndmask_b32_e32 v1, 0, v209, vcc
	v_cmp_gt_i32_e32 vcc, s63, v148
	s_nop 1
	v_cndmask_b32_e32 v3, 0, v210, vcc
	v_cmp_gt_i32_e32 vcc, s63, v149
	s_nop 1
	v_cndmask_b32_e32 v2, 0, v211, vcc

.LBB0_4344:
	v_cndmask_b32_e64 v0, 0, 1, s[38:39]
	v_cmp_ne_u32_e64 s[2:3], 1, v0
	s_andn2_b64 vcc, exec, s[38:39]
	v_mov_b32_e32 v158, v140
	v_mov_b32_e32 v155, v134
	v_mov_b32_e32 v156, v136
	v_mov_b32_e32 v157, v138
	s_cbranch_vccnz .LBB0_4354
	v_add_u32_e32 v200, s61, v146
	v_cmp_gt_i32_e32 vcc, s62, v146
	v_mov_b32_e32 v201, s61
	s_nop 0
	v_cndmask_b32_e32 v200, v201, v200, vcc
	v_ashrrev_i32_e32 v201, 31, v200
	v_lshl_add_u64 v[200:201], v[200:201], 2, s[8:9]
	v_add_u32_e32 v202, s61, v147
	v_cmp_gt_i32_e32 vcc, s62, v147
	v_mov_b32_e32 v203, s61
	s_nop 0
	v_cndmask_b32_e32 v202, v203, v202, vcc
	v_ashrrev_i32_e32 v203, 31, v202
	v_lshl_add_u64 v[202:203], v[202:203], 2, s[8:9]
	v_add_u32_e32 v204, s61, v148
	v_cmp_gt_i32_e32 vcc, s62, v148
	v_mov_b32_e32 v205, s61
	s_nop 0
	v_cndmask_b32_e32 v204, v205, v204, vcc
	v_ashrrev_i32_e32 v205, 31, v204
	v_lshl_add_u64 v[204:205], v[204:205], 2, s[8:9]
	v_add_u32_e32 v206, s61, v149
	v_cmp_gt_i32_e32 vcc, s62, v149
	v_mov_b32_e32 v207, s61
	s_nop 0
	v_cndmask_b32_e32 v206, v207, v206, vcc
	v_ashrrev_i32_e32 v207, 31, v206
	v_lshl_add_u64 v[206:207], v[206:207], 2, s[8:9]
	global_load_dword v208, v[200:201], off
	global_load_dword v209, v[202:203], off
	global_load_dword v210, v[204:205], off
	global_load_dword v211, v[206:207], off
	s_waitcnt vmcnt(0)
	v_lshlrev_b32_e32 v208, 10, v208
	v_lshlrev_b32_e32 v209, 10, v209
	v_lshlrev_b32_e32 v210, 10, v210
	v_lshlrev_b32_e32 v211, 10, v211
	v_and_b32_e32 v208, 0x3fff800, v208
	v_and_b32_e32 v209, 0x3fff800, v209
	v_and_b32_e32 v210, 0x3fff800, v210
	v_and_b32_e32 v211, 0x3fff800, v211
	v_cmp_gt_i32_e32 vcc, s62, v146
	s_nop 1
	v_cndmask_b32_e32 v0, 0, v208, vcc
	v_cmp_gt_i32_e32 vcc, s62, v147
	s_nop 1
	v_cndmask_b32_e32 v1, 0, v209, vcc
	v_cmp_gt_i32_e32 vcc, s62, v148
	s_nop 1
	v_cndmask_b32_e32 v3, 0, v210, vcc
	v_cmp_gt_i32_e32 vcc, s62, v149
	s_nop 1
	v_cndmask_b32_e32 v2, 0, v211, vcc
